# RWKV state pass: static s_setprio 3 for its two computing waves, reset after the pass (on top of v102)
# speedup vs baseline: 1.0061x; 1.0061x over previous
.LBB0_918:
	s_andn2_b64 vcc, exec, s[0:1]
	s_cbranch_vccnz .LBB0_1047
	s_mov_b32 s14, s85
	s_mov_b32 s0, s62
	s_mov_b64 s[6:7], s[86:87]
	s_load_dwordx2 s[8:9], s[6:7], 0x138
	s_waitcnt vmcnt(0)
	v_mbcnt_lo_u32_b32 v0, s0, 0
	v_mbcnt_hi_u32_b32 v118, s0, v0
	v_readlane_b32 s0, v251, 17
	v_readlane_b32 s1, v251, 18
	s_waitcnt vmcnt(1)
	v_and_b32_e32 v160, 31, v118
	s_andn2_b64 vcc, exec, s[0:1]
	s_cbranch_vccnz .LBB0_945
	s_cmp_lt_u32 s14, 2
	s_cbranch_scc0 .Lscan_pr
	s_setprio 3
.Lscan_pr:
	s_cmp_gt_i32 s14, 3
	s_cselect_b64 s[4:5], -1, 0
	s_lshl_b32 s0, s14, 3
	s_sub_i32 s10, s0, 32
	s_mov_b64 s[2:3], -1
	s_and_b64 vcc, exec, s[4:5]
	s_cbranch_vccnz .LBB0_922
	s_lshl_b32 s0, s10, 10
	s_ashr_i32 s1, s0, 31
	s_mov_b64 s[2:3], 0

.LBB0_945:
	s_setprio 0
	s_movk_i32 s0, 0x5f
	v_cmp_lt_i32_e32 vcc, s0, v118
	s_and_saveexec_b64 s[0:1], vcc
	s_xor_b64 s[0:1], exec, s[0:1]
	s_or_saveexec_b64 s[0:1], s[0:1]
	v_mov_b32_e32 v5, 0
	v_mov_b32_e32 v162, s27
	v_mov_b32_e32 v4, 0
	s_xor_b64 exec, exec, s[0:1]
	s_cbranch_execz .LBB0_949
	s_load_dwordx4 s[16:19], s[6:7], 0x90
	v_readlane_b32 s2, v253, 27
	v_subrev_u32_e32 v6, 64, v118
	v_mov_b32_e32 v5, 0
	v_add_u32_e32 v0, s2, v118
	v_ashrrev_i32_e32 v1, 31, v0
	v_lshlrev_b64 v[2:3], 2, v[0:1]
	s_waitcnt lgkmcnt(0)
	v_lshl_add_u64 v[0:1], s[18:19], 0, v[2:3]
	v_lshl_add_u64 v[2:3], s[16:17], 0, v[2:3]
	s_mov_b64 s[2:3], 0
	v_mov_b32_e32 v4, 0
